# speedup vs baseline: 1.0062x; 1.0062x over previous
_Z5k_mixPKhPKfPhi:
	s_load_dwordx4 s[4:7], s[0:1], 0x0
	s_load_dwordx2 s[8:9], s[0:1], 0x10
	s_load_dword s10, s[0:1], 0x18
	v_lshl_or_b32 v1, s2, 8, v0
	v_lshlrev_b32_e32 v2, 4, v1
	v_lshrrev_b32_e32 v3, 5, v1
	s_mov_b32 s28, 0x41800000
	s_mov_b32 s30, 0x41000000
	s_waitcnt lgkmcnt(0)
	v_add_u32_e32 v3, s10, v3
	v_lshlrev_b32_e32 v3, 5, v3
	s_add_u32 s26, s6, 0x80000
	s_addc_u32 s27, s7, 0
	s_add_u32 s12, s4, 0x800000
	s_addc_u32 s13, s5, 0
	s_add_u32 s14, s12, 0x800000
	s_addc_u32 s15, s13, 0
	s_add_u32 s16, s14, 0x800000
	s_addc_u32 s17, s15, 0
	s_add_u32 s18, s16, 0x800000
	s_addc_u32 s19, s17, 0
	s_add_u32 s20, s18, 0x800000
	s_addc_u32 s21, s19, 0
	s_add_u32 s22, s20, 0x800000
	s_addc_u32 s23, s21, 0
	s_add_u32 s24, s22, 0x800000
	s_addc_u32 s25, s23, 0
	s_add_u32 s32, s8, 0x800000
	s_addc_u32 s33, s9, 0
	global_load_dwordx4 v[100:103], v3, s[6:7]
	global_load_dwordx4 v[104:107], v3, s[6:7] offset:16
	global_load_dwordx4 v[108:111], v3, s[26:27]
	global_load_dwordx4 v[112:115], v3, s[26:27] offset:16
	global_load_dwordx4 v[68:71], v2, s[4:5] nt
	global_load_dwordx4 v[72:75], v2, s[12:13] nt
	global_load_dwordx4 v[76:79], v2, s[14:15] nt
	global_load_dwordx4 v[80:83], v2, s[16:17] nt
	global_load_dwordx4 v[84:87], v2, s[18:19] nt
	global_load_dwordx4 v[88:91], v2, s[20:21] nt
	global_load_dwordx4 v[92:95], v2, s[22:23] nt
	global_load_dwordx4 v[96:99], v2, s[24:25] nt
	v_lshl_add_u32 v1, s10, 9, v2
	s_waitcnt vmcnt(8)
	v_pk_mul_f32 v[100:101], v[100:101], s[28:29] op_sel_hi:[1,0]
	v_pk_mul_f32 v[102:103], v[102:103], s[28:29] op_sel_hi:[1,0]
	v_pk_mul_f32 v[104:105], v[104:105], s[28:29] op_sel_hi:[1,0]
	v_pk_mul_f32 v[106:107], v[106:107], s[28:29] op_sel_hi:[1,0]
	v_pk_mul_f32 v[108:109], v[108:109], s[28:29] op_sel_hi:[1,0]
	v_pk_mul_f32 v[110:111], v[110:111], s[28:29] op_sel_hi:[1,0]
	v_pk_mul_f32 v[112:113], v[112:113], s[28:29] op_sel_hi:[1,0]
	v_pk_mul_f32 v[114:115], v[114:115], s[28:29] op_sel_hi:[1,0]
	s_waitcnt vmcnt(7)
	v_cvt_scalef32_pk_f32_fp4 v[116:117], v68, 1.0
	v_cvt_scalef32_pk_f32_fp4 v[118:119], v68, 1.0 op_sel:[1,0,0]
	v_cvt_scalef32_pk_f32_fp4 v[120:121], v68, 1.0 op_sel:[0,1,0]
	v_cvt_scalef32_pk_f32_fp4 v[122:123], v68, 1.0 op_sel:[1,1,0]
	v_pk_mul_f32 v[4:5], v[116:117], v[100:101] op_sel_hi:[1,0]
	v_pk_mul_f32 v[36:37], v[116:117], v[108:109] op_sel_hi:[1,0]
	v_pk_mul_f32 v[6:7], v[118:119], v[100:101] op_sel_hi:[1,0]
	v_pk_mul_f32 v[38:39], v[118:119], v[108:109] op_sel_hi:[1,0]
	v_pk_mul_f32 v[8:9], v[120:121], v[100:101] op_sel_hi:[1,0]
	v_pk_mul_f32 v[40:41], v[120:121], v[108:109] op_sel_hi:[1,0]
	v_pk_mul_f32 v[10:11], v[122:123], v[100:101] op_sel_hi:[1,0]
	v_pk_mul_f32 v[42:43], v[122:123], v[108:109] op_sel_hi:[1,0]
	v_cvt_scalef32_pk_f32_fp4 v[116:117], v69, 1.0
	v_cvt_scalef32_pk_f32_fp4 v[118:119], v69, 1.0 op_sel:[1,0,0]
	v_cvt_scalef32_pk_f32_fp4 v[120:121], v69, 1.0 op_sel:[0,1,0]
	v_cvt_scalef32_pk_f32_fp4 v[122:123], v69, 1.0 op_sel:[1,1,0]
	v_pk_mul_f32 v[12:13], v[116:117], v[100:101] op_sel_hi:[1,0]
	v_pk_mul_f32 v[44:45], v[116:117], v[108:109] op_sel_hi:[1,0]
	v_pk_mul_f32 v[14:15], v[118:119], v[100:101] op_sel_hi:[1,0]
	v_pk_mul_f32 v[46:47], v[118:119], v[108:109] op_sel_hi:[1,0]
	v_pk_mul_f32 v[16:17], v[120:121], v[100:101] op_sel_hi:[1,0]
	v_pk_mul_f32 v[48:49], v[120:121], v[108:109] op_sel_hi:[1,0]
	v_pk_mul_f32 v[18:19], v[122:123], v[100:101] op_sel_hi:[1,0]
	v_pk_mul_f32 v[50:51], v[122:123], v[108:109] op_sel_hi:[1,0]
	v_cvt_scalef32_pk_f32_fp4 v[116:117], v70, 1.0
	v_cvt_scalef32_pk_f32_fp4 v[118:119], v70, 1.0 op_sel:[1,0,0]
	v_cvt_scalef32_pk_f32_fp4 v[120:121], v70, 1.0 op_sel:[0,1,0]
	v_cvt_scalef32_pk_f32_fp4 v[122:123], v70, 1.0 op_sel:[1,1,0]
	v_pk_mul_f32 v[20:21], v[116:117], v[100:101] op_sel_hi:[1,0]
	v_pk_mul_f32 v[52:53], v[116:117], v[108:109] op_sel_hi:[1,0]
	v_pk_mul_f32 v[22:23], v[118:119], v[100:101] op_sel_hi:[1,0]
	v_pk_mul_f32 v[54:55], v[118:119], v[108:109] op_sel_hi:[1,0]
	v_pk_mul_f32 v[24:25], v[120:121], v[100:101] op_sel_hi:[1,0]
	v_pk_mul_f32 v[56:57], v[120:121], v[108:109] op_sel_hi:[1,0]
	v_pk_mul_f32 v[26:27], v[122:123], v[100:101] op_sel_hi:[1,0]
	v_pk_mul_f32 v[58:59], v[122:123], v[108:109] op_sel_hi:[1,0]
	v_cvt_scalef32_pk_f32_fp4 v[116:117], v71, 1.0
	v_cvt_scalef32_pk_f32_fp4 v[118:119], v71, 1.0 op_sel:[1,0,0]
	v_cvt_scalef32_pk_f32_fp4 v[120:121], v71, 1.0 op_sel:[0,1,0]
	v_cvt_scalef32_pk_f32_fp4 v[122:123], v71, 1.0 op_sel:[1,1,0]
	v_pk_mul_f32 v[28:29], v[116:117], v[100:101] op_sel_hi:[1,0]
	v_pk_mul_f32 v[60:61], v[116:117], v[108:109] op_sel_hi:[1,0]
	v_pk_mul_f32 v[30:31], v[118:119], v[100:101] op_sel_hi:[1,0]
	v_pk_mul_f32 v[62:63], v[118:119], v[108:109] op_sel_hi:[1,0]
	v_pk_mul_f32 v[32:33], v[120:121], v[100:101] op_sel_hi:[1,0]
	v_pk_mul_f32 v[64:65], v[120:121], v[108:109] op_sel_hi:[1,0]
	v_pk_mul_f32 v[34:35], v[122:123], v[100:101] op_sel_hi:[1,0]
	v_pk_mul_f32 v[66:67], v[122:123], v[108:109] op_sel_hi:[1,0]
	s_waitcnt vmcnt(6)
	v_cvt_scalef32_pk_f32_fp4 v[116:117], v72, 1.0
	v_cvt_scalef32_pk_f32_fp4 v[118:119], v72, 1.0 op_sel:[1,0,0]
	v_cvt_scalef32_pk_f32_fp4 v[120:121], v72, 1.0 op_sel:[0,1,0]
	v_cvt_scalef32_pk_f32_fp4 v[122:123], v72, 1.0 op_sel:[1,1,0]
	v_pk_fma_f32 v[4:5], v[116:117], v[100:101], v[4:5] op_sel:[0,1,0] op_sel_hi:[1,1,1]
	v_pk_fma_f32 v[36:37], v[116:117], v[108:109], v[36:37] op_sel:[0,1,0] op_sel_hi:[1,1,1]
	v_pk_fma_f32 v[6:7], v[118:119], v[100:101], v[6:7] op_sel:[0,1,0] op_sel_hi:[1,1,1]
	v_pk_fma_f32 v[38:39], v[118:119], v[108:109], v[38:39] op_sel:[0,1,0] op_sel_hi:[1,1,1]
	v_pk_fma_f32 v[8:9], v[120:121], v[100:101], v[8:9] op_sel:[0,1,0] op_sel_hi:[1,1,1]
	v_pk_fma_f32 v[40:41], v[120:121], v[108:109], v[40:41] op_sel:[0,1,0] op_sel_hi:[1,1,1]
	v_pk_fma_f32 v[10:11], v[122:123], v[100:101], v[10:11] op_sel:[0,1,0] op_sel_hi:[1,1,1]
	v_pk_fma_f32 v[42:43], v[122:123], v[108:109], v[42:43] op_sel:[0,1,0] op_sel_hi:[1,1,1]
	v_cvt_scalef32_pk_f32_fp4 v[116:117], v73, 1.0
	v_cvt_scalef32_pk_f32_fp4 v[118:119], v73, 1.0 op_sel:[1,0,0]
	v_cvt_scalef32_pk_f32_fp4 v[120:121], v73, 1.0 op_sel:[0,1,0]
	v_cvt_scalef32_pk_f32_fp4 v[122:123], v73, 1.0 op_sel:[1,1,0]
	v_pk_fma_f32 v[12:13], v[116:117], v[100:101], v[12:13] op_sel:[0,1,0] op_sel_hi:[1,1,1]
	v_pk_fma_f32 v[44:45], v[116:117], v[108:109], v[44:45] op_sel:[0,1,0] op_sel_hi:[1,1,1]
	v_pk_fma_f32 v[14:15], v[118:119], v[100:101], v[14:15] op_sel:[0,1,0] op_sel_hi:[1,1,1]
	v_pk_fma_f32 v[46:47], v[118:119], v[108:109], v[46:47] op_sel:[0,1,0] op_sel_hi:[1,1,1]
	v_pk_fma_f32 v[16:17], v[120:121], v[100:101], v[16:17] op_sel:[0,1,0] op_sel_hi:[1,1,1]
	v_pk_fma_f32 v[48:49], v[120:121], v[108:109], v[48:49] op_sel:[0,1,0] op_sel_hi:[1,1,1]
	v_pk_fma_f32 v[18:19], v[122:123], v[100:101], v[18:19] op_sel:[0,1,0] op_sel_hi:[1,1,1]
	v_pk_fma_f32 v[50:51], v[122:123], v[108:109], v[50:51] op_sel:[0,1,0] op_sel_hi:[1,1,1]
	v_cvt_scalef32_pk_f32_fp4 v[116:117], v74, 1.0
	v_cvt_scalef32_pk_f32_fp4 v[118:119], v74, 1.0 op_sel:[1,0,0]
	v_cvt_scalef32_pk_f32_fp4 v[120:121], v74, 1.0 op_sel:[0,1,0]
	v_cvt_scalef32_pk_f32_fp4 v[122:123], v74, 1.0 op_sel:[1,1,0]
	v_pk_fma_f32 v[20:21], v[116:117], v[100:101], v[20:21] op_sel:[0,1,0] op_sel_hi:[1,1,1]
	v_pk_fma_f32 v[52:53], v[116:117], v[108:109], v[52:53] op_sel:[0,1,0] op_sel_hi:[1,1,1]
	v_pk_fma_f32 v[22:23], v[118:119], v[100:101], v[22:23] op_sel:[0,1,0] op_sel_hi:[1,1,1]
	v_pk_fma_f32 v[54:55], v[118:119], v[108:109], v[54:55] op_sel:[0,1,0] op_sel_hi:[1,1,1]
	v_pk_fma_f32 v[24:25], v[120:121], v[100:101], v[24:25] op_sel:[0,1,0] op_sel_hi:[1,1,1]
	v_pk_fma_f32 v[56:57], v[120:121], v[108:109], v[56:57] op_sel:[0,1,0] op_sel_hi:[1,1,1]
	v_pk_fma_f32 v[26:27], v[122:123], v[100:101], v[26:27] op_sel:[0,1,0] op_sel_hi:[1,1,1]
	v_pk_fma_f32 v[58:59], v[122:123], v[108:109], v[58:59] op_sel:[0,1,0] op_sel_hi:[1,1,1]
	v_cvt_scalef32_pk_f32_fp4 v[116:117], v75, 1.0
	v_cvt_scalef32_pk_f32_fp4 v[118:119], v75, 1.0 op_sel:[1,0,0]
	v_cvt_scalef32_pk_f32_fp4 v[120:121], v75, 1.0 op_sel:[0,1,0]
	v_cvt_scalef32_pk_f32_fp4 v[122:123], v75, 1.0 op_sel:[1,1,0]
	v_pk_fma_f32 v[28:29], v[116:117], v[100:101], v[28:29] op_sel:[0,1,0] op_sel_hi:[1,1,1]
	v_pk_fma_f32 v[60:61], v[116:117], v[108:109], v[60:61] op_sel:[0,1,0] op_sel_hi:[1,1,1]
	v_pk_fma_f32 v[30:31], v[118:119], v[100:101], v[30:31] op_sel:[0,1,0] op_sel_hi:[1,1,1]
	v_pk_fma_f32 v[62:63], v[118:119], v[108:109], v[62:63] op_sel:[0,1,0] op_sel_hi:[1,1,1]
	v_pk_fma_f32 v[32:33], v[120:121], v[100:101], v[32:33] op_sel:[0,1,0] op_sel_hi:[1,1,1]
	v_pk_fma_f32 v[64:65], v[120:121], v[108:109], v[64:65] op_sel:[0,1,0] op_sel_hi:[1,1,1]
	v_pk_fma_f32 v[34:35], v[122:123], v[100:101], v[34:35] op_sel:[0,1,0] op_sel_hi:[1,1,1]
	v_pk_fma_f32 v[66:67], v[122:123], v[108:109], v[66:67] op_sel:[0,1,0] op_sel_hi:[1,1,1]
	s_waitcnt vmcnt(5)
	v_cvt_scalef32_pk_f32_fp4 v[116:117], v76, 1.0
	v_cvt_scalef32_pk_f32_fp4 v[118:119], v76, 1.0 op_sel:[1,0,0]
	v_cvt_scalef32_pk_f32_fp4 v[120:121], v76, 1.0 op_sel:[0,1,0]
	v_cvt_scalef32_pk_f32_fp4 v[122:123], v76, 1.0 op_sel:[1,1,0]
	v_pk_fma_f32 v[4:5], v[116:117], v[102:103], v[4:5] op_sel_hi:[1,0,1]
	v_pk_fma_f32 v[36:37], v[116:117], v[110:111], v[36:37] op_sel_hi:[1,0,1]
	v_pk_fma_f32 v[6:7], v[118:119], v[102:103], v[6:7] op_sel_hi:[1,0,1]
	v_pk_fma_f32 v[38:39], v[118:119], v[110:111], v[38:39] op_sel_hi:[1,0,1]
	v_pk_fma_f32 v[8:9], v[120:121], v[102:103], v[8:9] op_sel_hi:[1,0,1]
	v_pk_fma_f32 v[40:41], v[120:121], v[110:111], v[40:41] op_sel_hi:[1,0,1]
	v_pk_fma_f32 v[10:11], v[122:123], v[102:103], v[10:11] op_sel_hi:[1,0,1]
	v_pk_fma_f32 v[42:43], v[122:123], v[110:111], v[42:43] op_sel_hi:[1,0,1]
	v_cvt_scalef32_pk_f32_fp4 v[116:117], v77, 1.0
	v_cvt_scalef32_pk_f32_fp4 v[118:119], v77, 1.0 op_sel:[1,0,0]
	v_cvt_scalef32_pk_f32_fp4 v[120:121], v77, 1.0 op_sel:[0,1,0]
	v_cvt_scalef32_pk_f32_fp4 v[122:123], v77, 1.0 op_sel:[1,1,0]
	v_pk_fma_f32 v[12:13], v[116:117], v[102:103], v[12:13] op_sel_hi:[1,0,1]
	v_pk_fma_f32 v[44:45], v[116:117], v[110:111], v[44:45] op_sel_hi:[1,0,1]
	v_pk_fma_f32 v[14:15], v[118:119], v[102:103], v[14:15] op_sel_hi:[1,0,1]
	v_pk_fma_f32 v[46:47], v[118:119], v[110:111], v[46:47] op_sel_hi:[1,0,1]
	v_pk_fma_f32 v[16:17], v[120:121], v[102:103], v[16:17] op_sel_hi:[1,0,1]
	v_pk_fma_f32 v[48:49], v[120:121], v[110:111], v[48:49] op_sel_hi:[1,0,1]
	v_pk_fma_f32 v[18:19], v[122:123], v[102:103], v[18:19] op_sel_hi:[1,0,1]
	v_pk_fma_f32 v[50:51], v[122:123], v[110:111], v[50:51] op_sel_hi:[1,0,1]
	v_cvt_scalef32_pk_f32_fp4 v[116:117], v78, 1.0
	v_cvt_scalef32_pk_f32_fp4 v[118:119], v78, 1.0 op_sel:[1,0,0]
	v_cvt_scalef32_pk_f32_fp4 v[120:121], v78, 1.0 op_sel:[0,1,0]
	v_cvt_scalef32_pk_f32_fp4 v[122:123], v78, 1.0 op_sel:[1,1,0]
	v_pk_fma_f32 v[20:21], v[116:117], v[102:103], v[20:21] op_sel_hi:[1,0,1]
	v_pk_fma_f32 v[52:53], v[116:117], v[110:111], v[52:53] op_sel_hi:[1,0,1]
	v_pk_fma_f32 v[22:23], v[118:119], v[102:103], v[22:23] op_sel_hi:[1,0,1]
	v_pk_fma_f32 v[54:55], v[118:119], v[110:111], v[54:55] op_sel_hi:[1,0,1]
	v_pk_fma_f32 v[24:25], v[120:121], v[102:103], v[24:25] op_sel_hi:[1,0,1]
	v_pk_fma_f32 v[56:57], v[120:121], v[110:111], v[56:57] op_sel_hi:[1,0,1]
	v_pk_fma_f32 v[26:27], v[122:123], v[102:103], v[26:27] op_sel_hi:[1,0,1]
	v_pk_fma_f32 v[58:59], v[122:123], v[110:111], v[58:59] op_sel_hi:[1,0,1]
	v_cvt_scalef32_pk_f32_fp4 v[116:117], v79, 1.0
	v_cvt_scalef32_pk_f32_fp4 v[118:119], v79, 1.0 op_sel:[1,0,0]
	v_cvt_scalef32_pk_f32_fp4 v[120:121], v79, 1.0 op_sel:[0,1,0]
	v_cvt_scalef32_pk_f32_fp4 v[122:123], v79, 1.0 op_sel:[1,1,0]
	v_pk_fma_f32 v[28:29], v[116:117], v[102:103], v[28:29] op_sel_hi:[1,0,1]
	v_pk_fma_f32 v[60:61], v[116:117], v[110:111], v[60:61] op_sel_hi:[1,0,1]
	v_pk_fma_f32 v[30:31], v[118:119], v[102:103], v[30:31] op_sel_hi:[1,0,1]
	v_pk_fma_f32 v[62:63], v[118:119], v[110:111], v[62:63] op_sel_hi:[1,0,1]
	v_pk_fma_f32 v[32:33], v[120:121], v[102:103], v[32:33] op_sel_hi:[1,0,1]
	v_pk_fma_f32 v[64:65], v[120:121], v[110:111], v[64:65] op_sel_hi:[1,0,1]
	v_pk_fma_f32 v[34:35], v[122:123], v[102:103], v[34:35] op_sel_hi:[1,0,1]
	v_pk_fma_f32 v[66:67], v[122:123], v[110:111], v[66:67] op_sel_hi:[1,0,1]
	s_waitcnt vmcnt(4)
	v_cvt_scalef32_pk_f32_fp4 v[116:117], v80, 1.0
	v_cvt_scalef32_pk_f32_fp4 v[118:119], v80, 1.0 op_sel:[1,0,0]
	v_cvt_scalef32_pk_f32_fp4 v[120:121], v80, 1.0 op_sel:[0,1,0]
	v_cvt_scalef32_pk_f32_fp4 v[122:123], v80, 1.0 op_sel:[1,1,0]
	v_pk_fma_f32 v[4:5], v[116:117], v[102:103], v[4:5] op_sel:[0,1,0] op_sel_hi:[1,1,1]
	v_pk_fma_f32 v[36:37], v[116:117], v[110:111], v[36:37] op_sel:[0,1,0] op_sel_hi:[1,1,1]
	v_pk_fma_f32 v[6:7], v[118:119], v[102:103], v[6:7] op_sel:[0,1,0] op_sel_hi:[1,1,1]
	v_pk_fma_f32 v[38:39], v[118:119], v[110:111], v[38:39] op_sel:[0,1,0] op_sel_hi:[1,1,1]
	v_pk_fma_f32 v[8:9], v[120:121], v[102:103], v[8:9] op_sel:[0,1,0] op_sel_hi:[1,1,1]
	v_pk_fma_f32 v[40:41], v[120:121], v[110:111], v[40:41] op_sel:[0,1,0] op_sel_hi:[1,1,1]
	v_pk_fma_f32 v[10:11], v[122:123], v[102:103], v[10:11] op_sel:[0,1,0] op_sel_hi:[1,1,1]
	v_pk_fma_f32 v[42:43], v[122:123], v[110:111], v[42:43] op_sel:[0,1,0] op_sel_hi:[1,1,1]
	v_cvt_scalef32_pk_f32_fp4 v[116:117], v81, 1.0
	v_cvt_scalef32_pk_f32_fp4 v[118:119], v81, 1.0 op_sel:[1,0,0]
	v_cvt_scalef32_pk_f32_fp4 v[120:121], v81, 1.0 op_sel:[0,1,0]
	v_cvt_scalef32_pk_f32_fp4 v[122:123], v81, 1.0 op_sel:[1,1,0]
	v_pk_fma_f32 v[12:13], v[116:117], v[102:103], v[12:13] op_sel:[0,1,0] op_sel_hi:[1,1,1]
	v_pk_fma_f32 v[44:45], v[116:117], v[110:111], v[44:45] op_sel:[0,1,0] op_sel_hi:[1,1,1]
	v_pk_fma_f32 v[14:15], v[118:119], v[102:103], v[14:15] op_sel:[0,1,0] op_sel_hi:[1,1,1]
	v_pk_fma_f32 v[46:47], v[118:119], v[110:111], v[46:47] op_sel:[0,1,0] op_sel_hi:[1,1,1]
	v_pk_fma_f32 v[16:17], v[120:121], v[102:103], v[16:17] op_sel:[0,1,0] op_sel_hi:[1,1,1]
	v_pk_fma_f32 v[48:49], v[120:121], v[110:111], v[48:49] op_sel:[0,1,0] op_sel_hi:[1,1,1]
	v_pk_fma_f32 v[18:19], v[122:123], v[102:103], v[18:19] op_sel:[0,1,0] op_sel_hi:[1,1,1]
	v_pk_fma_f32 v[50:51], v[122:123], v[110:111], v[50:51] op_sel:[0,1,0] op_sel_hi:[1,1,1]
	v_cvt_scalef32_pk_f32_fp4 v[116:117], v82, 1.0
	v_cvt_scalef32_pk_f32_fp4 v[118:119], v82, 1.0 op_sel:[1,0,0]
	v_cvt_scalef32_pk_f32_fp4 v[120:121], v82, 1.0 op_sel:[0,1,0]
	v_cvt_scalef32_pk_f32_fp4 v[122:123], v82, 1.0 op_sel:[1,1,0]
	v_pk_fma_f32 v[20:21], v[116:117], v[102:103], v[20:21] op_sel:[0,1,0] op_sel_hi:[1,1,1]
	v_pk_fma_f32 v[52:53], v[116:117], v[110:111], v[52:53] op_sel:[0,1,0] op_sel_hi:[1,1,1]
	v_pk_fma_f32 v[22:23], v[118:119], v[102:103], v[22:23] op_sel:[0,1,0] op_sel_hi:[1,1,1]
	v_pk_fma_f32 v[54:55], v[118:119], v[110:111], v[54:55] op_sel:[0,1,0] op_sel_hi:[1,1,1]
	v_pk_fma_f32 v[24:25], v[120:121], v[102:103], v[24:25] op_sel:[0,1,0] op_sel_hi:[1,1,1]
	v_pk_fma_f32 v[56:57], v[120:121], v[110:111], v[56:57] op_sel:[0,1,0] op_sel_hi:[1,1,1]
	v_pk_fma_f32 v[26:27], v[122:123], v[102:103], v[26:27] op_sel:[0,1,0] op_sel_hi:[1,1,1]
	v_pk_fma_f32 v[58:59], v[122:123], v[110:111], v[58:59] op_sel:[0,1,0] op_sel_hi:[1,1,1]
	v_cvt_scalef32_pk_f32_fp4 v[116:117], v83, 1.0
	v_cvt_scalef32_pk_f32_fp4 v[118:119], v83, 1.0 op_sel:[1,0,0]
	v_cvt_scalef32_pk_f32_fp4 v[120:121], v83, 1.0 op_sel:[0,1,0]
	v_cvt_scalef32_pk_f32_fp4 v[122:123], v83, 1.0 op_sel:[1,1,0]
	v_pk_fma_f32 v[28:29], v[116:117], v[102:103], v[28:29] op_sel:[0,1,0] op_sel_hi:[1,1,1]
	v_pk_fma_f32 v[60:61], v[116:117], v[110:111], v[60:61] op_sel:[0,1,0] op_sel_hi:[1,1,1]
	v_pk_fma_f32 v[30:31], v[118:119], v[102:103], v[30:31] op_sel:[0,1,0] op_sel_hi:[1,1,1]
	v_pk_fma_f32 v[62:63], v[118:119], v[110:111], v[62:63] op_sel:[0,1,0] op_sel_hi:[1,1,1]
	v_pk_fma_f32 v[32:33], v[120:121], v[102:103], v[32:33] op_sel:[0,1,0] op_sel_hi:[1,1,1]
	v_pk_fma_f32 v[64:65], v[120:121], v[110:111], v[64:65] op_sel:[0,1,0] op_sel_hi:[1,1,1]
	v_pk_fma_f32 v[34:35], v[122:123], v[102:103], v[34:35] op_sel:[0,1,0] op_sel_hi:[1,1,1]
	v_pk_fma_f32 v[66:67], v[122:123], v[110:111], v[66:67] op_sel:[0,1,0] op_sel_hi:[1,1,1]
	s_waitcnt vmcnt(3)
	v_cvt_scalef32_pk_f32_fp4 v[116:117], v84, 1.0
	v_cvt_scalef32_pk_f32_fp4 v[118:119], v84, 1.0 op_sel:[1,0,0]
	v_cvt_scalef32_pk_f32_fp4 v[120:121], v84, 1.0 op_sel:[0,1,0]
	v_cvt_scalef32_pk_f32_fp4 v[122:123], v84, 1.0 op_sel:[1,1,0]
	v_pk_fma_f32 v[4:5], v[116:117], v[104:105], v[4:5] op_sel_hi:[1,0,1]
	v_pk_fma_f32 v[36:37], v[116:117], v[112:113], v[36:37] op_sel_hi:[1,0,1]
	v_pk_fma_f32 v[6:7], v[118:119], v[104:105], v[6:7] op_sel_hi:[1,0,1]
	v_pk_fma_f32 v[38:39], v[118:119], v[112:113], v[38:39] op_sel_hi:[1,0,1]
	v_pk_fma_f32 v[8:9], v[120:121], v[104:105], v[8:9] op_sel_hi:[1,0,1]
	v_pk_fma_f32 v[40:41], v[120:121], v[112:113], v[40:41] op_sel_hi:[1,0,1]
	v_pk_fma_f32 v[10:11], v[122:123], v[104:105], v[10:11] op_sel_hi:[1,0,1]
	v_pk_fma_f32 v[42:43], v[122:123], v[112:113], v[42:43] op_sel_hi:[1,0,1]
	v_cvt_scalef32_pk_f32_fp4 v[116:117], v85, 1.0
	v_cvt_scalef32_pk_f32_fp4 v[118:119], v85, 1.0 op_sel:[1,0,0]
	v_cvt_scalef32_pk_f32_fp4 v[120:121], v85, 1.0 op_sel:[0,1,0]
	v_cvt_scalef32_pk_f32_fp4 v[122:123], v85, 1.0 op_sel:[1,1,0]
	v_pk_fma_f32 v[12:13], v[116:117], v[104:105], v[12:13] op_sel_hi:[1,0,1]
	v_pk_fma_f32 v[44:45], v[116:117], v[112:113], v[44:45] op_sel_hi:[1,0,1]
	v_pk_fma_f32 v[14:15], v[118:119], v[104:105], v[14:15] op_sel_hi:[1,0,1]
	v_pk_fma_f32 v[46:47], v[118:119], v[112:113], v[46:47] op_sel_hi:[1,0,1]
	v_pk_fma_f32 v[16:17], v[120:121], v[104:105], v[16:17] op_sel_hi:[1,0,1]
	v_pk_fma_f32 v[48:49], v[120:121], v[112:113], v[48:49] op_sel_hi:[1,0,1]
	v_pk_fma_f32 v[18:19], v[122:123], v[104:105], v[18:19] op_sel_hi:[1,0,1]
	v_pk_fma_f32 v[50:51], v[122:123], v[112:113], v[50:51] op_sel_hi:[1,0,1]
	v_cvt_scalef32_pk_f32_fp4 v[116:117], v86, 1.0
	v_cvt_scalef32_pk_f32_fp4 v[118:119], v86, 1.0 op_sel:[1,0,0]
	v_cvt_scalef32_pk_f32_fp4 v[120:121], v86, 1.0 op_sel:[0,1,0]
	v_cvt_scalef32_pk_f32_fp4 v[122:123], v86, 1.0 op_sel:[1,1,0]
	v_pk_fma_f32 v[20:21], v[116:117], v[104:105], v[20:21] op_sel_hi:[1,0,1]
	v_pk_fma_f32 v[52:53], v[116:117], v[112:113], v[52:53] op_sel_hi:[1,0,1]
	v_pk_fma_f32 v[22:23], v[118:119], v[104:105], v[22:23] op_sel_hi:[1,0,1]
	v_pk_fma_f32 v[54:55], v[118:119], v[112:113], v[54:55] op_sel_hi:[1,0,1]
	v_pk_fma_f32 v[24:25], v[120:121], v[104:105], v[24:25] op_sel_hi:[1,0,1]
	v_pk_fma_f32 v[56:57], v[120:121], v[112:113], v[56:57] op_sel_hi:[1,0,1]
	v_pk_fma_f32 v[26:27], v[122:123], v[104:105], v[26:27] op_sel_hi:[1,0,1]
	v_pk_fma_f32 v[58:59], v[122:123], v[112:113], v[58:59] op_sel_hi:[1,0,1]
	v_cvt_scalef32_pk_f32_fp4 v[116:117], v87, 1.0
	v_cvt_scalef32_pk_f32_fp4 v[118:119], v87, 1.0 op_sel:[1,0,0]
	v_cvt_scalef32_pk_f32_fp4 v[120:121], v87, 1.0 op_sel:[0,1,0]
	v_cvt_scalef32_pk_f32_fp4 v[122:123], v87, 1.0 op_sel:[1,1,0]
	v_pk_fma_f32 v[28:29], v[116:117], v[104:105], v[28:29] op_sel_hi:[1,0,1]
	v_pk_fma_f32 v[60:61], v[116:117], v[112:113], v[60:61] op_sel_hi:[1,0,1]
	v_pk_fma_f32 v[30:31], v[118:119], v[104:105], v[30:31] op_sel_hi:[1,0,1]
	v_pk_fma_f32 v[62:63], v[118:119], v[112:113], v[62:63] op_sel_hi:[1,0,1]
	v_pk_fma_f32 v[32:33], v[120:121], v[104:105], v[32:33] op_sel_hi:[1,0,1]
	v_pk_fma_f32 v[64:65], v[120:121], v[112:113], v[64:65] op_sel_hi:[1,0,1]
	v_pk_fma_f32 v[34:35], v[122:123], v[104:105], v[34:35] op_sel_hi:[1,0,1]
	v_pk_fma_f32 v[66:67], v[122:123], v[112:113], v[66:67] op_sel_hi:[1,0,1]
	s_waitcnt vmcnt(2)
	v_cvt_scalef32_pk_f32_fp4 v[116:117], v88, 1.0
	v_cvt_scalef32_pk_f32_fp4 v[118:119], v88, 1.0 op_sel:[1,0,0]
	v_cvt_scalef32_pk_f32_fp4 v[120:121], v88, 1.0 op_sel:[0,1,0]
	v_cvt_scalef32_pk_f32_fp4 v[122:123], v88, 1.0 op_sel:[1,1,0]
	v_pk_fma_f32 v[4:5], v[116:117], v[104:105], v[4:5] op_sel:[0,1,0] op_sel_hi:[1,1,1]
	v_pk_fma_f32 v[36:37], v[116:117], v[112:113], v[36:37] op_sel:[0,1,0] op_sel_hi:[1,1,1]
	v_pk_fma_f32 v[6:7], v[118:119], v[104:105], v[6:7] op_sel:[0,1,0] op_sel_hi:[1,1,1]
	v_pk_fma_f32 v[38:39], v[118:119], v[112:113], v[38:39] op_sel:[0,1,0] op_sel_hi:[1,1,1]
	v_pk_fma_f32 v[8:9], v[120:121], v[104:105], v[8:9] op_sel:[0,1,0] op_sel_hi:[1,1,1]
	v_pk_fma_f32 v[40:41], v[120:121], v[112:113], v[40:41] op_sel:[0,1,0] op_sel_hi:[1,1,1]
	v_pk_fma_f32 v[10:11], v[122:123], v[104:105], v[10:11] op_sel:[0,1,0] op_sel_hi:[1,1,1]
	v_pk_fma_f32 v[42:43], v[122:123], v[112:113], v[42:43] op_sel:[0,1,0] op_sel_hi:[1,1,1]
	v_cvt_scalef32_pk_f32_fp4 v[116:117], v89, 1.0
	v_cvt_scalef32_pk_f32_fp4 v[118:119], v89, 1.0 op_sel:[1,0,0]
	v_cvt_scalef32_pk_f32_fp4 v[120:121], v89, 1.0 op_sel:[0,1,0]
	v_cvt_scalef32_pk_f32_fp4 v[122:123], v89, 1.0 op_sel:[1,1,0]
	v_pk_fma_f32 v[12:13], v[116:117], v[104:105], v[12:13] op_sel:[0,1,0] op_sel_hi:[1,1,1]
	v_pk_fma_f32 v[44:45], v[116:117], v[112:113], v[44:45] op_sel:[0,1,0] op_sel_hi:[1,1,1]
	v_pk_fma_f32 v[14:15], v[118:119], v[104:105], v[14:15] op_sel:[0,1,0] op_sel_hi:[1,1,1]
	v_pk_fma_f32 v[46:47], v[118:119], v[112:113], v[46:47] op_sel:[0,1,0] op_sel_hi:[1,1,1]
	v_pk_fma_f32 v[16:17], v[120:121], v[104:105], v[16:17] op_sel:[0,1,0] op_sel_hi:[1,1,1]
	v_pk_fma_f32 v[48:49], v[120:121], v[112:113], v[48:49] op_sel:[0,1,0] op_sel_hi:[1,1,1]
	v_pk_fma_f32 v[18:19], v[122:123], v[104:105], v[18:19] op_sel:[0,1,0] op_sel_hi:[1,1,1]
	v_pk_fma_f32 v[50:51], v[122:123], v[112:113], v[50:51] op_sel:[0,1,0] op_sel_hi:[1,1,1]
	v_cvt_scalef32_pk_f32_fp4 v[116:117], v90, 1.0
	v_cvt_scalef32_pk_f32_fp4 v[118:119], v90, 1.0 op_sel:[1,0,0]
	v_cvt_scalef32_pk_f32_fp4 v[120:121], v90, 1.0 op_sel:[0,1,0]
	v_cvt_scalef32_pk_f32_fp4 v[122:123], v90, 1.0 op_sel:[1,1,0]
	v_pk_fma_f32 v[20:21], v[116:117], v[104:105], v[20:21] op_sel:[0,1,0] op_sel_hi:[1,1,1]
	v_pk_fma_f32 v[52:53], v[116:117], v[112:113], v[52:53] op_sel:[0,1,0] op_sel_hi:[1,1,1]
	v_pk_fma_f32 v[22:23], v[118:119], v[104:105], v[22:23] op_sel:[0,1,0] op_sel_hi:[1,1,1]
	v_pk_fma_f32 v[54:55], v[118:119], v[112:113], v[54:55] op_sel:[0,1,0] op_sel_hi:[1,1,1]
	v_pk_fma_f32 v[24:25], v[120:121], v[104:105], v[24:25] op_sel:[0,1,0] op_sel_hi:[1,1,1]
	v_pk_fma_f32 v[56:57], v[120:121], v[112:113], v[56:57] op_sel:[0,1,0] op_sel_hi:[1,1,1]
	v_pk_fma_f32 v[26:27], v[122:123], v[104:105], v[26:27] op_sel:[0,1,0] op_sel_hi:[1,1,1]
	v_pk_fma_f32 v[58:59], v[122:123], v[112:113], v[58:59] op_sel:[0,1,0] op_sel_hi:[1,1,1]
	v_cvt_scalef32_pk_f32_fp4 v[116:117], v91, 1.0
	v_cvt_scalef32_pk_f32_fp4 v[118:119], v91, 1.0 op_sel:[1,0,0]
	v_cvt_scalef32_pk_f32_fp4 v[120:121], v91, 1.0 op_sel:[0,1,0]
	v_cvt_scalef32_pk_f32_fp4 v[122:123], v91, 1.0 op_sel:[1,1,0]
	v_pk_fma_f32 v[28:29], v[116:117], v[104:105], v[28:29] op_sel:[0,1,0] op_sel_hi:[1,1,1]
	v_pk_fma_f32 v[60:61], v[116:117], v[112:113], v[60:61] op_sel:[0,1,0] op_sel_hi:[1,1,1]
	v_pk_fma_f32 v[30:31], v[118:119], v[104:105], v[30:31] op_sel:[0,1,0] op_sel_hi:[1,1,1]
	v_pk_fma_f32 v[62:63], v[118:119], v[112:113], v[62:63] op_sel:[0,1,0] op_sel_hi:[1,1,1]
	v_pk_fma_f32 v[32:33], v[120:121], v[104:105], v[32:33] op_sel:[0,1,0] op_sel_hi:[1,1,1]
	v_pk_fma_f32 v[64:65], v[120:121], v[112:113], v[64:65] op_sel:[0,1,0] op_sel_hi:[1,1,1]
	v_pk_fma_f32 v[34:35], v[122:123], v[104:105], v[34:35] op_sel:[0,1,0] op_sel_hi:[1,1,1]
	v_pk_fma_f32 v[66:67], v[122:123], v[112:113], v[66:67] op_sel:[0,1,0] op_sel_hi:[1,1,1]
	s_waitcnt vmcnt(1)
	v_cvt_scalef32_pk_f32_fp4 v[116:117], v92, 1.0
	v_cvt_scalef32_pk_f32_fp4 v[118:119], v92, 1.0 op_sel:[1,0,0]
	v_cvt_scalef32_pk_f32_fp4 v[120:121], v92, 1.0 op_sel:[0,1,0]
	v_cvt_scalef32_pk_f32_fp4 v[122:123], v92, 1.0 op_sel:[1,1,0]
	v_pk_fma_f32 v[4:5], v[116:117], v[106:107], v[4:5] op_sel_hi:[1,0,1]
	v_pk_fma_f32 v[36:37], v[116:117], v[114:115], v[36:37] op_sel_hi:[1,0,1]
	v_pk_fma_f32 v[6:7], v[118:119], v[106:107], v[6:7] op_sel_hi:[1,0,1]
	v_pk_fma_f32 v[38:39], v[118:119], v[114:115], v[38:39] op_sel_hi:[1,0,1]
	v_pk_fma_f32 v[8:9], v[120:121], v[106:107], v[8:9] op_sel_hi:[1,0,1]
	v_pk_fma_f32 v[40:41], v[120:121], v[114:115], v[40:41] op_sel_hi:[1,0,1]
	v_pk_fma_f32 v[10:11], v[122:123], v[106:107], v[10:11] op_sel_hi:[1,0,1]
	v_pk_fma_f32 v[42:43], v[122:123], v[114:115], v[42:43] op_sel_hi:[1,0,1]
	v_cvt_scalef32_pk_f32_fp4 v[116:117], v93, 1.0
	v_cvt_scalef32_pk_f32_fp4 v[118:119], v93, 1.0 op_sel:[1,0,0]
	v_cvt_scalef32_pk_f32_fp4 v[120:121], v93, 1.0 op_sel:[0,1,0]
	v_cvt_scalef32_pk_f32_fp4 v[122:123], v93, 1.0 op_sel:[1,1,0]
	v_pk_fma_f32 v[12:13], v[116:117], v[106:107], v[12:13] op_sel_hi:[1,0,1]
	v_pk_fma_f32 v[44:45], v[116:117], v[114:115], v[44:45] op_sel_hi:[1,0,1]
	v_pk_fma_f32 v[14:15], v[118:119], v[106:107], v[14:15] op_sel_hi:[1,0,1]
	v_pk_fma_f32 v[46:47], v[118:119], v[114:115], v[46:47] op_sel_hi:[1,0,1]
	v_pk_fma_f32 v[16:17], v[120:121], v[106:107], v[16:17] op_sel_hi:[1,0,1]
	v_pk_fma_f32 v[48:49], v[120:121], v[114:115], v[48:49] op_sel_hi:[1,0,1]
	v_pk_fma_f32 v[18:19], v[122:123], v[106:107], v[18:19] op_sel_hi:[1,0,1]
	v_pk_fma_f32 v[50:51], v[122:123], v[114:115], v[50:51] op_sel_hi:[1,0,1]
	v_cvt_scalef32_pk_f32_fp4 v[116:117], v94, 1.0
	v_cvt_scalef32_pk_f32_fp4 v[118:119], v94, 1.0 op_sel:[1,0,0]
	v_cvt_scalef32_pk_f32_fp4 v[120:121], v94, 1.0 op_sel:[0,1,0]
	v_cvt_scalef32_pk_f32_fp4 v[122:123], v94, 1.0 op_sel:[1,1,0]
	v_pk_fma_f32 v[20:21], v[116:117], v[106:107], v[20:21] op_sel_hi:[1,0,1]
	v_pk_fma_f32 v[52:53], v[116:117], v[114:115], v[52:53] op_sel_hi:[1,0,1]
	v_pk_fma_f32 v[22:23], v[118:119], v[106:107], v[22:23] op_sel_hi:[1,0,1]
	v_pk_fma_f32 v[54:55], v[118:119], v[114:115], v[54:55] op_sel_hi:[1,0,1]
	v_pk_fma_f32 v[24:25], v[120:121], v[106:107], v[24:25] op_sel_hi:[1,0,1]
	v_pk_fma_f32 v[56:57], v[120:121], v[114:115], v[56:57] op_sel_hi:[1,0,1]
	v_pk_fma_f32 v[26:27], v[122:123], v[106:107], v[26:27] op_sel_hi:[1,0,1]
	v_pk_fma_f32 v[58:59], v[122:123], v[114:115], v[58:59] op_sel_hi:[1,0,1]
	v_cvt_scalef32_pk_f32_fp4 v[116:117], v95, 1.0
	v_cvt_scalef32_pk_f32_fp4 v[118:119], v95, 1.0 op_sel:[1,0,0]
	v_cvt_scalef32_pk_f32_fp4 v[120:121], v95, 1.0 op_sel:[0,1,0]
	v_cvt_scalef32_pk_f32_fp4 v[122:123], v95, 1.0 op_sel:[1,1,0]
	v_pk_fma_f32 v[28:29], v[116:117], v[106:107], v[28:29] op_sel_hi:[1,0,1]
	v_pk_fma_f32 v[60:61], v[116:117], v[114:115], v[60:61] op_sel_hi:[1,0,1]
	v_pk_fma_f32 v[30:31], v[118:119], v[106:107], v[30:31] op_sel_hi:[1,0,1]
	v_pk_fma_f32 v[62:63], v[118:119], v[114:115], v[62:63] op_sel_hi:[1,0,1]
	v_pk_fma_f32 v[32:33], v[120:121], v[106:107], v[32:33] op_sel_hi:[1,0,1]
	v_pk_fma_f32 v[64:65], v[120:121], v[114:115], v[64:65] op_sel_hi:[1,0,1]
	v_pk_fma_f32 v[34:35], v[122:123], v[106:107], v[34:35] op_sel_hi:[1,0,1]
	v_pk_fma_f32 v[66:67], v[122:123], v[114:115], v[66:67] op_sel_hi:[1,0,1]
	s_waitcnt vmcnt(0)
	v_cvt_scalef32_pk_f32_fp4 v[116:117], v96, 1.0
	v_cvt_scalef32_pk_f32_fp4 v[118:119], v96, 1.0 op_sel:[1,0,0]
	v_cvt_scalef32_pk_f32_fp4 v[120:121], v96, 1.0 op_sel:[0,1,0]
	v_cvt_scalef32_pk_f32_fp4 v[122:123], v96, 1.0 op_sel:[1,1,0]
	v_pk_fma_f32 v[4:5], v[116:117], v[106:107], v[4:5] op_sel:[0,1,0] op_sel_hi:[1,1,1]
	v_pk_fma_f32 v[36:37], v[116:117], v[114:115], v[36:37] op_sel:[0,1,0] op_sel_hi:[1,1,1]
	v_pk_fma_f32 v[6:7], v[118:119], v[106:107], v[6:7] op_sel:[0,1,0] op_sel_hi:[1,1,1]
	v_pk_fma_f32 v[38:39], v[118:119], v[114:115], v[38:39] op_sel:[0,1,0] op_sel_hi:[1,1,1]
	v_pk_fma_f32 v[8:9], v[120:121], v[106:107], v[8:9] op_sel:[0,1,0] op_sel_hi:[1,1,1]
	v_pk_fma_f32 v[40:41], v[120:121], v[114:115], v[40:41] op_sel:[0,1,0] op_sel_hi:[1,1,1]
	v_pk_fma_f32 v[10:11], v[122:123], v[106:107], v[10:11] op_sel:[0,1,0] op_sel_hi:[1,1,1]
	v_pk_fma_f32 v[42:43], v[122:123], v[114:115], v[42:43] op_sel:[0,1,0] op_sel_hi:[1,1,1]
	v_cvt_scalef32_pk_f32_fp4 v[116:117], v97, 1.0
	v_cvt_scalef32_pk_f32_fp4 v[118:119], v97, 1.0 op_sel:[1,0,0]
	v_cvt_scalef32_pk_f32_fp4 v[120:121], v97, 1.0 op_sel:[0,1,0]
	v_cvt_scalef32_pk_f32_fp4 v[122:123], v97, 1.0 op_sel:[1,1,0]
	v_pk_fma_f32 v[12:13], v[116:117], v[106:107], v[12:13] op_sel:[0,1,0] op_sel_hi:[1,1,1]
	v_pk_fma_f32 v[44:45], v[116:117], v[114:115], v[44:45] op_sel:[0,1,0] op_sel_hi:[1,1,1]
	v_pk_fma_f32 v[14:15], v[118:119], v[106:107], v[14:15] op_sel:[0,1,0] op_sel_hi:[1,1,1]
	v_pk_fma_f32 v[46:47], v[118:119], v[114:115], v[46:47] op_sel:[0,1,0] op_sel_hi:[1,1,1]
	v_pk_fma_f32 v[16:17], v[120:121], v[106:107], v[16:17] op_sel:[0,1,0] op_sel_hi:[1,1,1]
	v_pk_fma_f32 v[48:49], v[120:121], v[114:115], v[48:49] op_sel:[0,1,0] op_sel_hi:[1,1,1]
	v_pk_fma_f32 v[18:19], v[122:123], v[106:107], v[18:19] op_sel:[0,1,0] op_sel_hi:[1,1,1]
	v_pk_fma_f32 v[50:51], v[122:123], v[114:115], v[50:51] op_sel:[0,1,0] op_sel_hi:[1,1,1]
	v_cvt_scalef32_pk_f32_fp4 v[116:117], v98, 1.0
	v_cvt_scalef32_pk_f32_fp4 v[118:119], v98, 1.0 op_sel:[1,0,0]
	v_cvt_scalef32_pk_f32_fp4 v[120:121], v98, 1.0 op_sel:[0,1,0]
	v_cvt_scalef32_pk_f32_fp4 v[122:123], v98, 1.0 op_sel:[1,1,0]
	v_pk_fma_f32 v[20:21], v[116:117], v[106:107], v[20:21] op_sel:[0,1,0] op_sel_hi:[1,1,1]
	v_pk_fma_f32 v[52:53], v[116:117], v[114:115], v[52:53] op_sel:[0,1,0] op_sel_hi:[1,1,1]
	v_pk_fma_f32 v[22:23], v[118:119], v[106:107], v[22:23] op_sel:[0,1,0] op_sel_hi:[1,1,1]
	v_pk_fma_f32 v[54:55], v[118:119], v[114:115], v[54:55] op_sel:[0,1,0] op_sel_hi:[1,1,1]
	v_pk_fma_f32 v[24:25], v[120:121], v[106:107], v[24:25] op_sel:[0,1,0] op_sel_hi:[1,1,1]
	v_pk_fma_f32 v[56:57], v[120:121], v[114:115], v[56:57] op_sel:[0,1,0] op_sel_hi:[1,1,1]
	v_pk_fma_f32 v[26:27], v[122:123], v[106:107], v[26:27] op_sel:[0,1,0] op_sel_hi:[1,1,1]
	v_pk_fma_f32 v[58:59], v[122:123], v[114:115], v[58:59] op_sel:[0,1,0] op_sel_hi:[1,1,1]
	v_cvt_scalef32_pk_f32_fp4 v[116:117], v99, 1.0
	v_cvt_scalef32_pk_f32_fp4 v[118:119], v99, 1.0 op_sel:[1,0,0]
	v_cvt_scalef32_pk_f32_fp4 v[120:121], v99, 1.0 op_sel:[0,1,0]
	v_cvt_scalef32_pk_f32_fp4 v[122:123], v99, 1.0 op_sel:[1,1,0]
	v_pk_fma_f32 v[28:29], v[116:117], v[106:107], v[28:29] op_sel:[0,1,0] op_sel_hi:[1,1,1]
	v_pk_fma_f32 v[60:61], v[116:117], v[114:115], v[60:61] op_sel:[0,1,0] op_sel_hi:[1,1,1]
	v_pk_fma_f32 v[30:31], v[118:119], v[106:107], v[30:31] op_sel:[0,1,0] op_sel_hi:[1,1,1]
	v_pk_fma_f32 v[62:63], v[118:119], v[114:115], v[62:63] op_sel:[0,1,0] op_sel_hi:[1,1,1]
	v_pk_fma_f32 v[32:33], v[120:121], v[106:107], v[32:33] op_sel:[0,1,0] op_sel_hi:[1,1,1]
	v_pk_fma_f32 v[64:65], v[120:121], v[114:115], v[64:65] op_sel:[0,1,0] op_sel_hi:[1,1,1]
	v_pk_fma_f32 v[34:35], v[122:123], v[106:107], v[34:35] op_sel:[0,1,0] op_sel_hi:[1,1,1]
	v_pk_fma_f32 v[66:67], v[122:123], v[114:115], v[66:67] op_sel:[0,1,0] op_sel_hi:[1,1,1]
	v_cvt_scalef32_pk_fp4_f32 v68, v4, v5, s30
	v_cvt_scalef32_pk_fp4_f32 v68, v6, v7, s30 op_sel:[0,0,1,0]
	v_cvt_scalef32_pk_fp4_f32 v68, v8, v9, s30 op_sel:[0,0,0,1]
	v_cvt_scalef32_pk_fp4_f32 v68, v10, v11, s30 op_sel:[0,0,1,1]
	v_cvt_scalef32_pk_fp4_f32 v69, v12, v13, s30
	v_cvt_scalef32_pk_fp4_f32 v69, v14, v15, s30 op_sel:[0,0,1,0]
	v_cvt_scalef32_pk_fp4_f32 v69, v16, v17, s30 op_sel:[0,0,0,1]
	v_cvt_scalef32_pk_fp4_f32 v69, v18, v19, s30 op_sel:[0,0,1,1]
	v_cvt_scalef32_pk_fp4_f32 v70, v20, v21, s30
	v_cvt_scalef32_pk_fp4_f32 v70, v22, v23, s30 op_sel:[0,0,1,0]
	v_cvt_scalef32_pk_fp4_f32 v70, v24, v25, s30 op_sel:[0,0,0,1]
	v_cvt_scalef32_pk_fp4_f32 v70, v26, v27, s30 op_sel:[0,0,1,1]
	v_cvt_scalef32_pk_fp4_f32 v71, v28, v29, s30
	v_cvt_scalef32_pk_fp4_f32 v71, v30, v31, s30 op_sel:[0,0,1,0]
	v_cvt_scalef32_pk_fp4_f32 v71, v32, v33, s30 op_sel:[0,0,0,1]
	v_cvt_scalef32_pk_fp4_f32 v71, v34, v35, s30 op_sel:[0,0,1,1]
	v_cvt_scalef32_pk_fp4_f32 v72, v36, v37, s30
	v_cvt_scalef32_pk_fp4_f32 v72, v38, v39, s30 op_sel:[0,0,1,0]
	v_cvt_scalef32_pk_fp4_f32 v72, v40, v41, s30 op_sel:[0,0,0,1]
	v_cvt_scalef32_pk_fp4_f32 v72, v42, v43, s30 op_sel:[0,0,1,1]
	v_cvt_scalef32_pk_fp4_f32 v73, v44, v45, s30
	v_cvt_scalef32_pk_fp4_f32 v73, v46, v47, s30 op_sel:[0,0,1,0]
	v_cvt_scalef32_pk_fp4_f32 v73, v48, v49, s30 op_sel:[0,0,0,1]
	v_cvt_scalef32_pk_fp4_f32 v73, v50, v51, s30 op_sel:[0,0,1,1]
	v_cvt_scalef32_pk_fp4_f32 v74, v52, v53, s30
	v_cvt_scalef32_pk_fp4_f32 v74, v54, v55, s30 op_sel:[0,0,1,0]
	v_cvt_scalef32_pk_fp4_f32 v74, v56, v57, s30 op_sel:[0,0,0,1]
	v_cvt_scalef32_pk_fp4_f32 v74, v58, v59, s30 op_sel:[0,0,1,1]
	v_cvt_scalef32_pk_fp4_f32 v75, v60, v61, s30
	v_cvt_scalef32_pk_fp4_f32 v75, v62, v63, s30 op_sel:[0,0,1,0]
	v_cvt_scalef32_pk_fp4_f32 v75, v64, v65, s30 op_sel:[0,0,0,1]
	v_cvt_scalef32_pk_fp4_f32 v75, v66, v67, s30 op_sel:[0,0,1,1]
	global_store_dwordx4 v1, v[68:71], s[8:9]
	global_store_dwordx4 v1, v[72:75], s[32:33]
	s_endpgm
